# speedup vs baseline: 1.0779x; 1.0268x over previous
_Z22k2_resolve_rank_gatherPKfS0_PKdS0_PKiPKyPKtS0_S4_Pf:
	s_load_dwordx16 s[4:19], s[0:1], 0x0
	s_load_dwordx4 s[20:23], s[0:1], 0x40
	s_and_b32 s3, s2, 7
	s_lshr_b32 s2, s2, 3
	s_lshl_b32 s3, s3, 7
	s_add_u32 s2, s2, s3
	v_and_b32_e32 v1, 0x3ff, v0
	s_lshr_b32 s24, s2, 6
	s_and_b32 s25, s2, 63
	s_lshl_b32 s26, s24, 9
	v_lshl_add_u32 v2, v1, 1, s26
	v_lshlrev_b32_e32 v3, 4, v2
	v_lshlrev_b32_e32 v24, 2, v2
	v_lshlrev_b32_e32 v25, 3, v2
	v_mov_b32_e32 v106, 0
	v_mov_b32_e32 v107, 0
	v_mov_b32_e32 v105, 0x1800
	v_lshlrev_b32_e32 v104, 3, v1
	s_movk_i32 s30, 0x641
	s_mov_b32 s32, 0xa0b5ed8d
	s_mov_b32 s33, 0x3ed0c6f7
	s_mov_b32 s34, 0xa0b5ed8d
	s_mov_b32 s35, 0xbed0c6f7
	s_mul_i32 s31, s26, 0x1904
	v_lshrrev_b32_e32 v29, 6, v1
	s_waitcnt lgkmcnt(0)
	global_load_dwordx4 v[4:7], v3, s[16:17]
	global_load_dwordx4 v[8:11], v3, s[16:17] offset:16
	global_load_dwordx2 v[12:13], v24, s[10:11]
	global_load_dwordx2 v[16:17], v24, s[12:13]
	global_load_dwordx4 v[20:23], v25, s[8:9]
	global_load_dwordx2 v[14:15], v24, s[18:19]
	global_load_dwordx2 v[18:19], v24, s[20:21]
	s_add_u32 s28, s4, s31
	s_addc_u32 s29, s5, 0
	v_readfirstlane_b32 s27, v29
	ds_write_b64 v105, v[106:107]
	ds_write_b64 v105, v[106:107] offset:8
	ds_write_b64 v105, v[106:107] offset:16
	ds_write_b64 v105, v[106:107] offset:24
	ds_write_b64 v104, v[106:107] offset:8448
	s_mov_b64 s[36:37], 0
	s_mov_b64 s[38:39], 0
	s_mov_b64 s[40:41], 0
	s_mov_b64 s[42:43], 0
	s_mov_b64 s[44:45], 0
	v_lshlrev_b32_e32 v2, 4, v1
	s_waitcnt vmcnt(2)
	ds_write_b128 v2, v[20:23] offset:12544
	v_lshlrev_b32_e32 v3, 5, v1
	ds_write_b128 v3, v[4:7] offset:22784
	ds_write_b128 v3, v[8:11] offset:22800
	ds_write_b64 v104, v[16:17] offset:30976
	v_and_b32_e32 v26, 0xffff, v4
	v_and_b32_e32 v27, 0xffff, v8
	v_max_u32_e32 v28, v26, v27
	v_cvt_f64_f32_e32 v[92:93], v12
	v_cvt_f64_f32_e32 v[94:95], v13
	v_add_f64 v[92:93], v[92:93], -v[20:21]
	v_add_f64 v[94:95], v[94:95], -v[22:23]
	ds_write_b128 v2, v[92:95] offset:0
	ds_write_b64 v104, v[12:13] offset:4096
	s_waitcnt vmcnt(0)
	ds_write_b64 v104, v[14:15] offset:33024
	v_cvt_f64_f32_e32 v[96:97], v14
	v_cvt_f64_f32_e32 v[98:99], v15
	v_add_f64 v[96:97], v[96:97], -v[20:21]
	v_add_f64 v[98:99], v[98:99], -v[22:23]
	s_waitcnt lgkmcnt(0)
	s_barrier
	v_cmp_lt_u32_e32 vcc, 0, v28
	s_cbranch_vccz .Lk2_l1_done
	v_cmp_lt_u32_e32 vcc, 0, v26
	s_and_saveexec_b64 s[46:47], vcc
	s_cbranch_execz .Lk2_l1_0_0
	v_lshrrev_b32_e32 v29, 16, v4
	v_mad_u32_u24 v30, v29, s30, v16
	v_lshlrev_b32_e32 v30, 2, v30
	v_lshlrev_b32_e32 v29, 3, v29
	global_load_dword v32, v30, s[28:29]
	ds_read_b64 v[34:35], v29 offset:12544

.Lk2_l1_done:
	v_lshrrev_b32_e32 v29, 5, v1
	v_and_b32_e32 v31, 31, v1
	v_lshl_add_u32 v29, s25, 3, v29
	v_lshlrev_b32_e32 v29, 3, v29
	v_lshlrev_b32_e32 v31, 3, v31
	ds_read_b64 v[116:117], v29 offset:0
	v_mov_b32_e32 v118, 0
	v_mov_b32_e32 v119, 0
	ds_read_b64 v[108:109], v31 offset:0
	ds_read_b64 v[110:111], v31 offset:256
	ds_read_b64 v[112:113], v31 offset:512
	ds_read_b64 v[114:115], v31 offset:768
	s_waitcnt lgkmcnt(0)
	v_add_f64 v[120:121], v[108:109], -v[116:117]
	v_cmp_lt_f64_e32 vcc, s[32:33], v[120:121]
	v_cmp_ge_f64_e64 s[48:49], s[32:33], |v[120:121]|
	s_nop 0
	v_addc_co_u32_e32 v118, vcc, 0, v118, vcc
	v_addc_co_u32_e64 v119, s[50:51], 0, v119, s[48:49]
	v_add_f64 v[120:121], v[110:111], -v[116:117]
	v_cmp_lt_f64_e32 vcc, s[32:33], v[120:121]
	v_cmp_ge_f64_e64 s[48:49], s[32:33], |v[120:121]|
	s_nop 0
	v_addc_co_u32_e32 v118, vcc, 0, v118, vcc
	v_addc_co_u32_e64 v119, s[50:51], 0, v119, s[48:49]
	v_add_f64 v[120:121], v[112:113], -v[116:117]
	v_cmp_lt_f64_e32 vcc, s[32:33], v[120:121]
	v_cmp_ge_f64_e64 s[48:49], s[32:33], |v[120:121]|
	s_nop 0
	v_addc_co_u32_e32 v118, vcc, 0, v118, vcc
	v_addc_co_u32_e64 v119, s[50:51], 0, v119, s[48:49]
	v_add_f64 v[120:121], v[114:115], -v[116:117]
	v_cmp_lt_f64_e32 vcc, s[32:33], v[120:121]
	v_cmp_ge_f64_e64 s[48:49], s[32:33], |v[120:121]|
	s_nop 0
	v_addc_co_u32_e32 v118, vcc, 0, v118, vcc
	v_addc_co_u32_e64 v119, s[50:51], 0, v119, s[48:49]
	ds_read_b64 v[108:109], v31 offset:1024
	ds_read_b64 v[110:111], v31 offset:1280
	ds_read_b64 v[112:113], v31 offset:1536
	ds_read_b64 v[114:115], v31 offset:1792
	s_waitcnt lgkmcnt(0)
	v_add_f64 v[120:121], v[108:109], -v[116:117]
	v_cmp_lt_f64_e32 vcc, s[32:33], v[120:121]
	v_cmp_ge_f64_e64 s[48:49], s[32:33], |v[120:121]|
	s_nop 0
	v_addc_co_u32_e32 v118, vcc, 0, v118, vcc
	v_addc_co_u32_e64 v119, s[50:51], 0, v119, s[48:49]
	v_add_f64 v[120:121], v[110:111], -v[116:117]
	v_cmp_lt_f64_e32 vcc, s[32:33], v[120:121]
	v_cmp_ge_f64_e64 s[48:49], s[32:33], |v[120:121]|
	s_nop 0
	v_addc_co_u32_e32 v118, vcc, 0, v118, vcc
	v_addc_co_u32_e64 v119, s[50:51], 0, v119, s[48:49]
	v_add_f64 v[120:121], v[112:113], -v[116:117]
	v_cmp_lt_f64_e32 vcc, s[32:33], v[120:121]
	v_cmp_ge_f64_e64 s[48:49], s[32:33], |v[120:121]|
	s_nop 0
	v_addc_co_u32_e32 v118, vcc, 0, v118, vcc
	v_addc_co_u32_e64 v119, s[50:51], 0, v119, s[48:49]
	v_add_f64 v[120:121], v[114:115], -v[116:117]
	v_cmp_lt_f64_e32 vcc, s[32:33], v[120:121]
	v_cmp_ge_f64_e64 s[48:49], s[32:33], |v[120:121]|
	s_nop 0
	v_addc_co_u32_e32 v118, vcc, 0, v118, vcc
	v_addc_co_u32_e64 v119, s[50:51], 0, v119, s[48:49]
	ds_read_b64 v[108:109], v31 offset:2048
	ds_read_b64 v[110:111], v31 offset:2304
	ds_read_b64 v[112:113], v31 offset:2560
	ds_read_b64 v[114:115], v31 offset:2816
	s_waitcnt lgkmcnt(0)
	v_add_f64 v[120:121], v[108:109], -v[116:117]
	v_cmp_lt_f64_e32 vcc, s[32:33], v[120:121]
	v_cmp_ge_f64_e64 s[48:49], s[32:33], |v[120:121]|
	s_nop 0
	v_addc_co_u32_e32 v118, vcc, 0, v118, vcc
	v_addc_co_u32_e64 v119, s[50:51], 0, v119, s[48:49]
	v_add_f64 v[120:121], v[110:111], -v[116:117]
	v_cmp_lt_f64_e32 vcc, s[32:33], v[120:121]
	v_cmp_ge_f64_e64 s[48:49], s[32:33], |v[120:121]|
	s_nop 0
	v_addc_co_u32_e32 v118, vcc, 0, v118, vcc
	v_addc_co_u32_e64 v119, s[50:51], 0, v119, s[48:49]
	v_add_f64 v[120:121], v[112:113], -v[116:117]
	v_cmp_lt_f64_e32 vcc, s[32:33], v[120:121]
	v_cmp_ge_f64_e64 s[48:49], s[32:33], |v[120:121]|
	s_nop 0
	v_addc_co_u32_e32 v118, vcc, 0, v118, vcc
	v_addc_co_u32_e64 v119, s[50:51], 0, v119, s[48:49]
	v_add_f64 v[120:121], v[114:115], -v[116:117]
	v_cmp_lt_f64_e32 vcc, s[32:33], v[120:121]
	v_cmp_ge_f64_e64 s[48:49], s[32:33], |v[120:121]|
	s_nop 0
	v_addc_co_u32_e32 v118, vcc, 0, v118, vcc
	v_addc_co_u32_e64 v119, s[50:51], 0, v119, s[48:49]
	ds_read_b64 v[108:109], v31 offset:3072
	ds_read_b64 v[110:111], v31 offset:3328
	ds_read_b64 v[112:113], v31 offset:3584
	ds_read_b64 v[114:115], v31 offset:3840
	s_waitcnt lgkmcnt(0)
	v_add_f64 v[120:121], v[108:109], -v[116:117]
	v_cmp_lt_f64_e32 vcc, s[32:33], v[120:121]
	v_cmp_ge_f64_e64 s[48:49], s[32:33], |v[120:121]|
	s_nop 0
	v_addc_co_u32_e32 v118, vcc, 0, v118, vcc
	v_addc_co_u32_e64 v119, s[50:51], 0, v119, s[48:49]
	v_add_f64 v[120:121], v[110:111], -v[116:117]
	v_cmp_lt_f64_e32 vcc, s[32:33], v[120:121]
	v_cmp_ge_f64_e64 s[48:49], s[32:33], |v[120:121]|
	s_nop 0
	v_addc_co_u32_e32 v118, vcc, 0, v118, vcc
	v_addc_co_u32_e64 v119, s[50:51], 0, v119, s[48:49]
	v_add_f64 v[120:121], v[112:113], -v[116:117]
	v_cmp_lt_f64_e32 vcc, s[32:33], v[120:121]
	v_cmp_ge_f64_e64 s[48:49], s[32:33], |v[120:121]|
	s_nop 0
	v_addc_co_u32_e32 v118, vcc, 0, v118, vcc
	v_addc_co_u32_e64 v119, s[50:51], 0, v119, s[48:49]
	v_add_f64 v[120:121], v[114:115], -v[116:117]
	v_cmp_lt_f64_e32 vcc, s[32:33], v[120:121]
	v_cmp_ge_f64_e64 s[48:49], s[32:33], |v[120:121]|
	s_nop 0
	v_addc_co_u32_e32 v118, vcc, 0, v118, vcc
	v_addc_co_u32_e64 v119, s[50:51], 0, v119, s[48:49]
	v_lshl_or_b32 v122, v119, 16, v118
	s_nop 1
	v_add_u32_dpp v122, v122, v122 quad_perm:[1,0,3,2] row_mask:0xf bank_mask:0xf
	s_nop 1
	v_add_u32_dpp v122, v122, v122 quad_perm:[2,3,0,1] row_mask:0xf bank_mask:0xf
	s_nop 1
	v_add_u32_dpp v122, v122, v122 row_half_mirror row_mask:0xf bank_mask:0xf
	s_nop 1
	v_add_u32_dpp v122, v122, v122 row_mirror row_mask:0xf bank_mask:0xf
	s_nop 1
	v_add_u32_dpp v122, v122, v122 row_bcast:15 row_mask:0xa bank_mask:0xf
	s_nop 1
	v_readlane_b32 s98, v122, 31
	v_readlane_b32 s99, v122, 63
	s_waitcnt vmcnt(0) lgkmcnt(0)
	v_cmp_lt_u32_e32 vcc, 0, v28
	s_cbranch_vccz .Lk2_l2_done
	v_cmp_lt_u32_e32 vcc, 0, v26
	s_and_saveexec_b64 s[46:47], vcc
	s_cbranch_execz .Lk2_l2_0_0
	v_cvt_f64_f32_e32 v[88:89], v32
	v_add_f64 v[88:89], v[88:89], -v[34:35]
	v_add_f64 v[88:89], v[88:89], -v[92:93]
	v_cmp_le_f64_e32 vcc, s[34:35], v[88:89]
	v_cmp_ge_f64_e64 s[48:49], s[32:33], v[88:89]
	s_or_b64 s[36:37], s[36:37], vcc
	s_and_b64 s[48:49], s[48:49], vcc
	s_or_b64 s[44:45], s[44:45], s[48:49]

.Lk2_t15_done1:
	s_or_b64 s[48:49], s[52:53], s[54:55]
	s_cmp_eq_u64 s[48:49], 0
	s_cbranch_scc1 .Lk2_nochg
	s_mov_b64 exec, s[52:53]
	ds_write_b64 v2, v[96:97] offset:0
	ds_write_b32 v104, v14 offset:4096
	s_mov_b64 exec, s[54:55]
	ds_write_b64 v2, v[98:99] offset:8
	ds_write_b32 v104, v15 offset:4100
	s_mov_b64 exec, -1
	v_mov_b32_e32 v30, 1
	ds_write_b32 v105, v30 offset:24

.Lk2_nohard:
	s_waitcnt lgkmcnt(0)
	s_barrier
	ds_read_b128 v[88:91], v105
	ds_read_b32 v100, v105 offset:24
	v_lshrrev_b32_e32 v29, 5, v1
	v_and_b32_e32 v31, 31, v1
	v_lshl_add_u32 v29, s25, 3, v29
	v_lshlrev_b32_e32 v29, 3, v29
	v_lshlrev_b32_e32 v31, 3, v31
	s_waitcnt lgkmcnt(0)
	v_readfirstlane_b32 s31, v90
	v_readfirstlane_b32 s74, v88
	s_cmp_lg_u32 s31, 0
	s_cbranch_scc1 .Lk2_fallback
	s_cmp_lg_u32 s74, 0
	s_cbranch_scc1 .Lk2_hard
	v_readfirstlane_b32 s31, v100
	s_cmp_lg_u32 s31, 0
	s_cbranch_scc1 .Lk2_rank
	s_mov_b32 s52, s98
	s_mov_b32 s53, s99
	s_branch .Lk2_ranked

.Lk2_ranked:
	v_and_b32_e32 v69, 63, v1
	v_lshlrev_b32_e32 v69, 4, v69
	v_add_u32_e32 v70, 0x1000, v69
	s_and_b32 s54, s52, 0xffff
	s_lshr_b32 s55, s52, 16
	s_and_b32 s56, s53, 0xffff
	s_lshr_b32 s57, s53, 16
	s_cmp_gt_u32 s55, 1
	s_cselect_b32 s58, 1, 0
	s_cmp_lt_u32 s54, 0x64
	s_cselect_b32 s59, 1, 0
	s_and_b32 s58, s58, s59
	s_cmp_gt_u32 s57, 1
	s_cselect_b32 s60, 1, 0
	s_cmp_lt_u32 s56, 0x64
	s_cselect_b32 s61, 1, 0
	s_and_b32 s60, s60, s61
	s_or_b32 s61, s58, s60
	s_lshl_b32 s62, s25, 3
	s_lshl_b32 s63, s27, 1
	s_add_u32 s62, s62, s63
	s_add_u32 s62, s62, s26
	s_lshl_b32 s62, s62, 13
	s_add_u32 s64, s6, s62
	s_addc_u32 s65, s7, 0
	s_add_u32 s66, s64, 0x2000
	s_addc_u32 s67, s65, 0
	s_cmp_lt_u32 s54, 0x64
	s_cbranch_scc0 .Lk2_ga_skip
	global_load_dwordx4 v[32:35], v69, s[64:65] offset:0 nt
	global_load_dwordx4 v[36:39], v69, s[64:65] offset:1024 nt
	global_load_dwordx4 v[40:43], v69, s[64:65] offset:2048 nt
	global_load_dwordx4 v[44:47], v69, s[64:65] offset:3072 nt
	global_load_dwordx4 v[48:51], v70, s[64:65] offset:0 nt
	global_load_dwordx4 v[52:55], v70, s[64:65] offset:1024 nt
	global_load_dwordx4 v[56:59], v70, s[64:65] offset:2048 nt
	global_load_dwordx4 v[60:63], v70, s[64:65] offset:3072 nt

.Lk2_needref:
	v_lshrrev_b32_e32 v29, 5, v1
	v_lshl_add_u32 v29, s25, 3, v29
	v_lshlrev_b32_e32 v29, 3, v29
	ds_read_b64 v[64:65], v29 offset:0
	s_cmp_lg_u32 s58, 0
	s_cselect_b32 s48, -1, 0
	s_cmp_lg_u32 s60, 0
	s_cselect_b32 s49, -1, 0
	s_mov_b64 exec, s[48:49]
	v_and_b32_e32 v29, 31, v1
	v_lshlrev_b32_e32 v30, 2, v29
	v_lshlrev_b32_e32 v29, 3, v29
	v_mov_b32_e32 v31, 1
	s_mov_b32 s3, 4
